# DeltaNet precompute item loop: next-item row/gate loads prefetched into registers, loop-invariant loads hoisted, dead 64-bit address math and never-taken rsqrt denormal scaling removed
# speedup vs baseline: 1.0330x; 1.0064x over previous
.LBB0_218:
	v_readlane_b32 s4, v253, 21
	s_cmpk_gt_i32 s30, 0x7ff
	v_readlane_b32 s5, v253, 22
	s_cbranch_scc1 .LBB0_347
	s_add_u32 s0, s88, 0x200000
	s_addc_u32 s1, s89, 0
	v_writelane_b32 v253, s0, 23
	s_movk_i32 s8, 0x110
	v_mbcnt_lo_u32_b32 v0, -1, 0
	v_writelane_b32 v253, s1, 24
	s_add_u32 s0, s88, 0x500000
	v_writelane_b32 v253, s0, 25
	s_addc_u32 s0, s89, 0
	v_writelane_b32 v253, s0, 26
	s_add_u32 s0, s60, 0x1000
	s_addc_u32 s1, s61, 0
	v_writelane_b32 v253, s0, 27
	v_mbcnt_hi_u32_b32 v209, -1, v0
	v_bfrev_b32_e32 v0, 0.5
	v_writelane_b32 v253, s1, 28
	s_add_u32 s0, s60, 0x1800
	s_addc_u32 s1, s61, 0
	v_writelane_b32 v253, s0, 29
	v_mov_b32_e32 v208, 0x3ecc95a3
	v_lshl_or_b32 v210, v209, 2, v0
	v_writelane_b32 v253, s1, 30
	s_add_u32 s0, s60, 0x2000
	s_addc_u32 s1, s61, 0
	v_writelane_b32 v253, s0, 31
	v_mov_b32_e32 v141, 0
	s_movk_i32 s11, 0x90
	v_writelane_b32 v253, s1, 32
	s_add_u32 s0, s60, 0x2800
	s_addc_u32 s1, s61, 0
	v_writelane_b32 v253, s0, 33
	v_mov_b32_e32 v142, 0x3f317218
	v_mov_b32_e32 v211, 0x7f800000
	v_writelane_b32 v253, s1, 34
	s_add_u32 s0, s60, 0x3000
	s_addc_u32 s1, s61, 0
	v_writelane_b32 v253, s0, 35
	v_mov_b32_e32 v212, 0x7fc00000
	v_mov_b32_e32 v213, 0xff800000
	v_writelane_b32 v253, s1, 36
	s_add_u32 s0, s60, 0x3800
	s_addc_u32 s1, s61, 0
	v_writelane_b32 v253, s0, 37
	v_mov_b32_e32 v214, 0x500
	s_mov_b32 s13, 0x800000
	v_writelane_b32 v253, s1, 38
	s_add_u32 s0, s60, 0x4000
	s_addc_u32 s1, s61, 0
	s_add_u32 s24, s60, 0x4800
	s_addc_u32 s25, s61, 0
	v_writelane_b32 v253, s0, 39
	s_add_u32 s26, s60, 0x5000
	s_addc_u32 s27, s61, 0
	v_writelane_b32 v253, s1, 40
	s_add_u32 s28, s60, 0x5800
	v_readlane_b32 s82, v253, 17
	s_addc_u32 s29, s61, 0
	s_lshl_b32 s95, s82, 3
	s_add_i32 s31, s95, -3
	s_add_i32 s52, s95, -2
	s_add_i32 s53, s95, -1
	s_or_b32 s54, s95, 1
	s_or_b32 s55, s95, 2
	s_or_b32 s33, s95, 3
	s_or_b32 s4, s95, 4
	s_or_b32 s5, s95, 5
	s_or_b32 s6, s95, 6
	s_or_b32 s7, s95, 7
	v_readlane_b32 s3, v253, 9
	s_cmp_lt_u32 s3, 64
	s_cselect_b64 s[0:1], -1, 0
	v_readlane_b32 s83, v253, 18
	v_writelane_b32 v253, s0, 41
	s_cmp_gt_u32 s3, 63
	s_mov_b32 s14, 0x5040100
	v_writelane_b32 v253, s1, 42
	s_cselect_b64 s[0:1], -1, 0
	v_writelane_b32 v253, s0, 43
	s_movk_i32 s16, 0x50
	s_mov_b32 s75, 0
	v_writelane_b32 v253, s1, 44
	s_mul_i32 s0, s54, 0x88
	s_add_i32 s1, s0, 0x88
	v_writelane_b32 v253, s1, 45
	s_add_i32 s1, s0, 0x110
	v_writelane_b32 v253, s1, 46
	s_add_i32 s1, s0, 0x198
	v_writelane_b32 v253, s1, 47
	s_add_i32 s1, s0, 0x220
	v_writelane_b32 v253, s1, 48
	s_add_i32 s1, s0, 0x2a8
	v_writelane_b32 v253, s1, 49
	s_addk_i32 s0, 0x330
	v_writelane_b32 v253, s0, 50
	s_bfe_u32 s0, s3, 0x20006
	s_cmpk_gt_u32 s3, 0xff
	s_cselect_b64 s[56:57], -1, 0
	s_add_i32 s1, 0, 0x4400
	s_lshl_b32 s9, s0, 4
	s_add_i32 s2, 0, 0x8800
	s_cmpk_lt_u32 s3, 0x100
	s_cselect_b32 s1, s1, 0
	v_writelane_b32 v253, s1, 51
	s_cselect_b32 s1, 0, s2
	v_writelane_b32 v253, s1, 52
	s_lshl_b32 s0, s0, 5
	s_lshl_b32 s10, s82, 4
	v_writelane_b32 v253, s0, 53
	s_or_b32 s0, s0, 16
	s_add_u32 s68, s88, 0xc400000
	s_addc_u32 s69, s89, 0
	s_add_u32 s72, s88, 0xe400000
	s_addc_u32 s73, s89, 0
	s_add_i32 s12, 0, 0x11400
	s_add_i32 s15, 0, 0x15c00
	s_add_i32 s17, 0, 0x1c800
	s_add_i32 s18, 0, 0x1a000
	s_add_i32 s19, 0, 0x1dc00
	s_mov_b32 s76, s30
	v_writelane_b32 v253, s0, 54
	s_mov_b32 s99, s76
	s_cmpk_lt_i32 s99, 0x800
	s_cbranch_scc0 .Lgpf_done_first
	v_readlane_b32 s100, v253, 17
	s_lshr_b32 s0, s99, 8
	s_lshl_b32 s0, s0, 12
	s_and_b32 s1, s99, 63
	s_lshl_b32 s101, s1, 6
	s_add_i32 s0, s0, s101
	s_or_b32 s1, s1, s100
	s_bfe_u32 s101, s99, 0x20006
	v_add_u32_e32 v219, s0, v237
	v_lshlrev_b32_e32 v219, 5, v219
	s_lshl_b32 s99, s101, 2
	v_add_u32_e32 v219, s99, v219
	s_lshl_b32 s100, s100, 3
	s_add_i32 s0, s0, s100
	s_lshl_b32 s0, s0, 10
	s_lshl_b32 s101, s101, 8
	s_add_i32 s0, s0, s101
	v_lshlrev_b32_e32 v217, 2, v237
	v_add_u32_e32 v217, s0, v217
	v_add_u32_e32 v218, 0x1000, v217
	s_add_u32 s100, s88, 0x200000
	s_addc_u32 s101, s89, 0
	s_cmp_eq_u32 s1, 0
	s_cbranch_scc1 .Lgpf_zero_first
	global_load_dword v172, v217, s[44:45] offset:-3072 nt
	global_load_dword v173, v217, s[68:69] offset:-3072 nt
	global_load_dword v174, v217, s[72:73] offset:-3072 nt
	global_load_dword v175, v217, s[44:45] offset:-2048 nt
	global_load_dword v176, v217, s[68:69] offset:-2048 nt
	global_load_dword v177, v217, s[72:73] offset:-2048 nt
	global_load_dword v178, v217, s[44:45] offset:-1024 nt
	global_load_dword v179, v217, s[68:69] offset:-1024 nt
	global_load_dword v180, v217, s[72:73] offset:-1024 nt
	s_branch .Lgpf_rest_first
.Lgpf_zero_first:
	v_mov_b32_e32 v172, 0
	v_mov_b32_e32 v173, 0
	v_mov_b32_e32 v174, 0
	v_mov_b32_e32 v175, 0
	v_mov_b32_e32 v176, 0
	v_mov_b32_e32 v177, 0
	v_mov_b32_e32 v178, 0
	v_mov_b32_e32 v179, 0
	v_mov_b32_e32 v180, 0
.Lgpf_rest_first:
	global_load_dword v181, v217, s[44:45] nt
	global_load_dword v182, v217, s[68:69] nt
	global_load_dword v183, v217, s[72:73] nt
	global_load_dword v184, v217, s[44:45] offset:1024 nt
	global_load_dword v185, v217, s[68:69] offset:1024 nt
	global_load_dword v186, v217, s[72:73] offset:1024 nt
	global_load_dword v187, v217, s[44:45] offset:2048 nt
	global_load_dword v188, v217, s[68:69] offset:2048 nt
	global_load_dword v189, v217, s[72:73] offset:2048 nt
	global_load_dword v190, v217, s[44:45] offset:3072 nt
	global_load_dword v191, v217, s[68:69] offset:3072 nt
	global_load_dword v192, v217, s[72:73] offset:3072 nt
	global_load_dword v193, v218, s[44:45] nt
	global_load_dword v194, v218, s[68:69] nt
	global_load_dword v195, v218, s[72:73] nt
	global_load_dword v196, v218, s[44:45] offset:1024 nt
	global_load_dword v197, v218, s[68:69] offset:1024 nt
	global_load_dword v198, v218, s[72:73] offset:1024 nt
	global_load_dword v199, v218, s[44:45] offset:2048 nt
	global_load_dword v200, v218, s[68:69] offset:2048 nt
	global_load_dword v201, v218, s[72:73] offset:2048 nt
	global_load_dword v202, v218, s[44:45] offset:3072 nt
	global_load_dword v203, v218, s[68:69] offset:3072 nt
	global_load_dword v204, v218, s[72:73] offset:3072 nt
	global_load_dword v205, v219, s[100:101]
	global_load_dword v206, v219, s[100:101] offset:16
.Lgpf_done_first:
	s_bfe_u32 s0, s76, 0x20006
	s_lshl_b32 s1, s0, 2
	v_mov_b32_e32 v217, s1
	global_load_dword v220, v217, s[64:65]
	global_load_dword v221, v217, s[62:63]
	v_lshlrev_b32_e32 v218, 1, v237
	v_lshl_add_u32 v218, s0, 7, v218
	v_lshlrev_b32_e32 v218, 2, v218
	global_load_dwordx2 v[222:223], v218, s[60:61]
	global_load_dwordx2 v[224:225], v218, s[60:61] offset:2048
	v_readlane_b32 s0, v253, 27
	v_readlane_b32 s1, v253, 28
	s_nop 4
	global_load_dwordx2 v[226:227], v218, s[0:1]
	v_readlane_b32 s0, v253, 29
	v_readlane_b32 s1, v253, 30
	s_nop 4
	global_load_dwordx2 v[228:229], v218, s[0:1]
	v_readlane_b32 s0, v253, 31
	v_readlane_b32 s1, v253, 32
	s_nop 4
	global_load_dwordx2 v[230:231], v218, s[0:1]
	v_readlane_b32 s0, v253, 33
	v_readlane_b32 s1, v253, 34
	s_nop 4
	global_load_dwordx2 v[232:233], v218, s[0:1]
	v_readlane_b32 s0, v253, 35
	v_readlane_b32 s1, v253, 36
	s_nop 4
	global_load_dwordx2 v[234:235], v218, s[0:1]
	v_readlane_b32 s0, v253, 37
	v_readlane_b32 s1, v253, 38
	s_nop 4
	global_load_dwordx2 v[238:239], v218, s[0:1]
	v_readlane_b32 s0, v253, 39
	v_readlane_b32 s1, v253, 40
	s_nop 4
	global_load_dwordx2 v[240:241], v218, s[0:1]
	global_load_dwordx2 v[242:243], v218, s[24:25]
	global_load_dwordx2 v[244:245], v218, s[26:27]
	global_load_dwordx2 v[246:247], v218, s[28:29]
	s_waitcnt vmcnt(0)
	s_branch .LBB0_221

.LBB0_221:
	s_memrealtime s[0:1]
	s_waitcnt vmcnt(8)
	s_lshl_b32 s100, s76, 4
	s_lshl_b32 s2, s76, 6
	s_and_b32 s100, s100, 0xfffff000
	s_and_b32 s2, s2, 0xfc0
	v_mov_b32_e32 v215, v237
	v_mov_b32_e32 v216, v236
	s_or_b32 s100, s100, s2
	v_readlane_b32 s20, v253, 23
	s_bfe_u32 s101, s76, 0x20006
	v_readlane_b32 s21, v253, 24
	s_lshl_b32 s74, s101, 2
	s_nop 0
	v_mov_b32_e32 v26, v205
	v_mov_b32_e32 v54, v206
	v_mov_b32_e32 v55, v220
	v_mov_b32_e32 v34, v221
	v_lshlrev_b32_e32 v38, 1, v215
	v_readlane_b32 s20, v253, 27
	v_readlane_b32 s21, v253, 28
	v_readlane_b32 s20, v253, 29
	v_readlane_b32 s21, v253, 30
	s_not_b32 s101, s2
	v_readlane_b32 s20, v253, 31
	v_readlane_b32 s21, v253, 32
	v_mov_b32_e32 v8, v222
	v_mov_b32_e32 v9, v223
	v_mov_b32_e32 v16, v224
	v_mov_b32_e32 v17, v225
	s_nop 0
	v_mov_b32_e32 v0, v226
	v_mov_b32_e32 v1, v227
	v_mov_b32_e32 v10, v228
	v_mov_b32_e32 v11, v229
	v_readlane_b32 s20, v253, 33
	v_readlane_b32 s21, v253, 34
	s_cmp_le_i32 s31, s101
	v_mov_b32_e32 v27, v141
	v_readlane_b32 s20, v253, 35
	v_readlane_b32 s21, v253, 36
	s_nop 1
	v_readlane_b32 s20, v253, 37
	v_readlane_b32 s21, v253, 38
	s_nop 1
	v_readlane_b32 s20, v253, 39
	v_readlane_b32 s21, v253, 40
	v_mov_b32_e32 v18, v230
	v_mov_b32_e32 v19, v231
	s_nop 0
	v_mov_b32_e32 v2, v232
	v_mov_b32_e32 v3, v233
	s_nop 0
	v_mov_b32_e32 v12, v234
	v_mov_b32_e32 v13, v235
	s_nop 0
	v_mov_b32_e32 v20, v238
	v_mov_b32_e32 v21, v239
	v_mov_b32_e32 v4, v240
	v_mov_b32_e32 v5, v241
	s_nop 0
	v_mov_b32_e32 v14, v242
	v_mov_b32_e32 v15, v243
	s_nop 0
	v_mov_b32_e32 v22, v244
	v_mov_b32_e32 v23, v245
	s_nop 0
	v_mov_b32_e32 v6, v246
	v_mov_b32_e32 v7, v247
	v_mov_b32_e32 v28, v141
	v_mov_b32_e32 v29, v141
	s_cbranch_scc1 .LBB0_223
	s_add_i32 s2, s100, s31
	s_ashr_i32 s3, s2, 31
	s_lshl_b64 s[2:3], s[2:3], 9
	v_mov_b32_e32 v27, v172
	v_mov_b32_e32 v28, v173
	s_nop 0
	v_mov_b32_e32 v29, v174
.LBB0_223:
	v_mov_b32_e32 v30, 0
	s_cmp_le_i32 s52, s101
	v_mov_b32_e32 v32, 0
	v_mov_b32_e32 v31, 0
	v_mov_b32_e32 v33, 0
	s_cbranch_scc1 .LBB0_225
	s_add_i32 s2, s100, s52
	s_ashr_i32 s3, s2, 31
	s_lshl_b64 s[2:3], s[2:3], 9
	v_mov_b32_e32 v31, v175
	v_mov_b32_e32 v32, v176
	s_nop 0
	v_mov_b32_e32 v33, v177
.LBB0_225:
	s_cmp_le_i32 s53, s101
	v_mov_b32_e32 v35, 0
	v_mov_b32_e32 v36, 0
	s_cbranch_scc1 .LBB0_227
	s_add_i32 s2, s100, s53
	s_ashr_i32 s3, s2, 31
	s_lshl_b64 s[2:3], s[2:3], 9
	v_mov_b32_e32 v35, v178
	v_mov_b32_e32 v30, v179
	s_nop 0
	v_mov_b32_e32 v36, v180
.LBB0_227:
	s_add_i32 s2, s100, s95
	s_ashr_i32 s3, s2, 31
	s_lshl_b64 s[2:3], s[2:3], 9
	s_add_i32 s2, s100, s54
	s_ashr_i32 s3, s2, 31
	v_mov_b32_e32 v37, v181
	s_lshl_b64 s[2:3], s[2:3], 9
	v_mov_b32_e32 v39, v182
	s_nop 0
	v_mov_b32_e32 v41, v183
	s_add_i32 s2, s100, s55
	s_ashr_i32 s3, s2, 31
	v_mov_b32_e32 v40, v184
	s_lshl_b64 s[2:3], s[2:3], 9
	v_mov_b32_e32 v42, v185
	s_nop 0
	v_mov_b32_e32 v43, v186
	s_add_i32 s2, s100, s33
	s_ashr_i32 s3, s2, 31
	s_lshl_b64 s[2:3], s[2:3], 9
	v_mov_b32_e32 v44, v187
	s_nop 0
	v_mov_b32_e32 v46, v188
	s_nop 0
	v_mov_b32_e32 v45, v189
	s_add_i32 s2, s100, s4
	s_ashr_i32 s3, s2, 31
	v_mov_b32_e32 v47, v190
	s_lshl_b64 s[2:3], s[2:3], 9
	v_mov_b32_e32 v48, v191
	s_nop 0
	v_mov_b32_e32 v49, v192
	s_add_i32 s2, s100, s5
	s_ashr_i32 s3, s2, 31
	s_lshl_b64 s[2:3], s[2:3], 9
	v_mov_b32_e32 v50, v193
	s_nop 0
	v_mov_b32_e32 v52, v194
	s_nop 0
	v_mov_b32_e32 v51, v195
	s_add_i32 s2, s100, s6
	s_ashr_i32 s3, s2, 31
	v_mov_b32_e32 v53, v196
	s_lshl_b64 s[2:3], s[2:3], 9
	s_add_i32 s100, s100, s7
	v_mov_b32_e32 v56, v197
	s_ashr_i32 s101, s100, 31
	v_mov_b32_e32 v57, v198
	s_lshl_b64 s[100:101], s[100:101], 9
	v_mov_b32_e32 v92, v199
	v_mov_b32_e32 v93, v200
	v_mov_b32_e32 v96, v201
	v_mov_b32_e32 v97, v202
	v_mov_b32_e32 v98, v203
	v_mov_b32_e32 v99, v204
	s_waitcnt lgkmcnt(0)
	v_add_f32_e32 v24, v54, v55
	s_mov_b32 s0, 0x41a00000
	v_cmp_nlt_f32_e32 vcc, s0, v24
	s_and_saveexec_b64 s[0:1], vcc
	s_cbranch_execz .LBB0_229
	v_mul_f32_e32 v24, 0x3fb8aa3b, v24
	v_exp_f32_e32 v68, v24
	s_mov_b32 s2, 0x3f2aaaab
	v_add_f32_e32 v54, 1.0, v68
	v_frexp_mant_f32_e32 v58, v54
	v_cvt_f64_f32_e32 v[24:25], v54
	v_frexp_exp_i32_f64_e32 v24, v[24:25]
	v_cmp_gt_f32_e32 vcc, s2, v58
	v_add_f32_e32 v55, -1.0, v54
	v_sub_f32_e32 v59, v55, v54
	v_subbrev_co_u32_e32 v62, vcc, 0, v24, vcc
	v_sub_u32_e32 v24, 0, v62
	v_sub_f32_e32 v55, v68, v55
	v_add_f32_e32 v59, 1.0, v59
	v_ldexp_f32 v25, v54, v24
	v_add_f32_e32 v55, v55, v59
	v_add_f32_e32 v54, -1.0, v25
	v_add_f32_e32 v58, 1.0, v25
	v_ldexp_f32 v24, v55, v24
	v_add_f32_e32 v55, 1.0, v54
	v_add_f32_e32 v59, -1.0, v58
	v_sub_f32_e32 v55, v25, v55
	v_sub_f32_e32 v25, v25, v59
	v_add_f32_e32 v55, v24, v55
	v_add_f32_e32 v24, v24, v25
	v_add_f32_e32 v63, v58, v24
	v_rcp_f32_e32 v65, v63
	v_sub_f32_e32 v25, v63, v58
	v_sub_f32_e32 v64, v24, v25
	v_add_f32_e32 v25, v54, v55
	v_mul_f32_e32 v67, v25, v65
	v_sub_f32_e32 v24, v25, v54
	v_mul_f32_e32 v54, v63, v67
	v_fma_f32 v58, v67, v63, -v54
	v_fmac_f32_e32 v58, v67, v64
	v_sub_f32_e32 v66, v55, v24
	v_add_f32_e32 v24, v54, v58
	v_sub_f32_e32 v55, v25, v24
	v_pk_add_f32 v[60:61], v[24:25], v[54:55] neg_lo:[0,1] neg_hi:[0,1]
	v_mov_b32_e32 v59, v24
	v_pk_add_f32 v[24:25], v[60:61], v[58:59] neg_lo:[0,1] neg_hi:[0,1]
	s_mov_b32 s2, 0x3f317218
	v_add_f32_e32 v25, v66, v25
	v_add_f32_e32 v24, v24, v25
	v_add_f32_e32 v25, v55, v24
	v_mul_f32_e32 v66, v65, v25
	v_mul_f32_e32 v54, v63, v66
	v_fma_f32 v58, v66, v63, -v54
	v_fmac_f32_e32 v58, v66, v64
	v_sub_f32_e32 v55, v55, v25
	v_add_f32_e32 v63, v24, v55
	v_add_f32_e32 v24, v54, v58
	v_sub_f32_e32 v55, v25, v24
	v_pk_add_f32 v[60:61], v[24:25], v[54:55] neg_lo:[0,1] neg_hi:[0,1]
	v_mov_b32_e32 v59, v24
	v_pk_add_f32 v[24:25], v[60:61], v[58:59] neg_lo:[0,1] neg_hi:[0,1]
	s_nop 0
	v_add_f32_e32 v25, v63, v25
	v_add_f32_e32 v24, v24, v25
	v_add_f32_e32 v25, v67, v66
	v_add_f32_e32 v24, v55, v24
	v_sub_f32_e32 v54, v25, v67
	v_mul_f32_e32 v24, v65, v24
	v_sub_f32_e32 v54, v66, v54
	v_add_f32_e32 v54, v54, v24
	v_add_f32_e32 v58, v25, v54
	v_mul_f32_e32 v59, v58, v58
	v_fmamk_f32 v24, v59, 0x3e9b6dac, v208
	v_fmaak_f32 v143, v59, v24, 0x3f2aaada
	v_cvt_f32_i32_e32 v24, v62
	v_sub_f32_e32 v25, v58, v25
	v_sub_f32_e32 v25, v54, v25
	v_ldexp_f32 v60, v25, 1
	v_mul_f32_e32 v25, v58, v59
	v_ldexp_f32 v55, v58, 1
	v_pk_mul_f32 v[58:59], v[24:25], v[142:143]
	s_nop 0
	v_fma_f32 v54, v24, s2, -v58
	v_fmac_f32_e32 v54, 0xb102e308, v24
	v_pk_add_f32 v[24:25], v[58:59], v[54:55]
	s_mov_b32 s2, 0x7f800000
	v_sub_f32_e32 v55, v25, v55
	v_sub_f32_e32 v55, v59, v55
	v_add_f32_e32 v61, v60, v55
	v_mov_b32_e32 v60, v58
	v_pk_add_f32 v[58:59], v[24:25], v[58:59] neg_lo:[0,1] neg_hi:[0,1]
	v_pk_add_f32 v[62:63], v[24:25], v[60:61]
	v_mov_b32_e32 v55, v24
	v_mov_b32_e32 v59, v63
	v_pk_add_f32 v[64:65], v[54:55], v[58:59] neg_lo:[0,1] neg_hi:[0,1]
	v_pk_add_f32 v[54:55], v[54:55], v[58:59]
	v_mov_b32_e32 v60, v61
	v_pk_add_f32 v[58:59], v[54:55], v[24:25] op_sel:[1,0] op_sel_hi:[0,1] neg_lo:[0,1] neg_hi:[0,1]
	v_pk_add_f32 v[66:67], v[62:63], v[58:59] op_sel_hi:[1,0] neg_lo:[0,1] neg_hi:[0,1]
	v_mov_b32_e32 v62, v63
	v_mov_b32_e32 v63, v55
	v_pk_mov_b32 v[58:59], v[24:25], v[58:59] op_sel:[1,0]
	v_mov_b32_e32 v61, v24
	v_pk_add_f32 v[58:59], v[62:63], v[58:59] neg_lo:[0,1] neg_hi:[0,1]
	v_mov_b32_e32 v66, v64
	v_pk_add_f32 v[24:25], v[60:61], v[58:59] neg_lo:[0,1] neg_hi:[0,1]
	v_mov_b32_e32 v65, v55
	v_pk_add_f32 v[58:59], v[66:67], v[24:25]
	v_cmp_neq_f32_e32 vcc, s2, v68
	v_pk_add_f32 v[60:61], v[58:59], v[58:59] op_sel:[0,1] op_sel_hi:[1,0]
	s_mov_b32 s2, 0x33800000
	v_pk_add_f32 v[54:55], v[54:55], v[60:61] op_sel:[1,0] op_sel_hi:[0,1]
	v_mov_b32_e32 v59, v54
	v_pk_add_f32 v[62:63], v[58:59], v[64:65] neg_lo:[0,1] neg_hi:[0,1]
	v_mov_b32_e32 v25, v60
	v_sub_f32_e32 v55, v58, v62
	v_pk_add_f32 v[24:25], v[24:25], v[62:63] neg_lo:[0,1] neg_hi:[0,1]
	v_sub_f32_e32 v55, v64, v55
	v_add_f32_e32 v24, v24, v55
	v_add_f32_e32 v24, v24, v25
	v_add_f32_e32 v24, v54, v24
	v_cndmask_b32_e32 v24, v211, v24, vcc
	v_cmp_ngt_f32_e32 vcc, -1.0, v68
	s_nop 1
	v_cndmask_b32_e32 v24, v212, v24, vcc
	v_cmp_neq_f32_e32 vcc, -1.0, v68
	s_nop 1
	v_cndmask_b32_e32 v24, v213, v24, vcc
	v_cmp_lt_f32_e64 vcc, |v68|, s2
	s_nop 1
	v_cndmask_b32_e32 v24, v24, v68, vcc
.LBB0_229:
	s_or_b64 exec, exec, s[0:1]
	v_mul_f32_e32 v25, 0x3fb8aa3b, v34
	v_exp_f32_e32 v25, v25
	v_and_b32_e32 v100, 64, v209
	v_mul_f32_e64 v54, v24, -v25
	v_readlane_b32 s0, v253, 41
	v_readlane_b32 s1, v253, 42
	s_ashr_i32 s77, s76, 31
	v_mov_b32_e32 v25, v54
	s_nop 1
	v_add_f32_dpp v25, v25, v25 row_shr:1 row_mask:0xf bank_mask:0xf
	s_nop 1
	v_add_f32_dpp v25, v25, v25 row_shr:2 row_mask:0xf bank_mask:0xf
	s_nop 1
	v_add_f32_dpp v25, v25, v25 row_shr:4 row_mask:0xf bank_mask:0xf
	s_nop 1
	v_add_f32_dpp v25, v25, v25 row_shr:8 row_mask:0xf bank_mask:0xf
	s_nop 1
	v_add_f32_dpp v25, v25, v25 row_bcast:15 row_mask:0xa bank_mask:0xf
	s_nop 1
	v_add_f32_dpp v25, v25, v25 row_bcast:31 row_mask:0xc bank_mask:0xf
	s_nop 1
	v_readlane_b32 s99, v25, 63
	s_nop 1
	v_mov_b32_e32 v24, s99
	v_mul_f32_e32 v34, 0x3fb8aa3b, v25
	v_exp_f32_e32 v94, v34
	s_andn2_b64 vcc, exec, s[0:1]
	s_cbranch_vccnz .LBB0_233
	s_waitcnt lgkmcnt(0)
	v_sub_f32_e32 v34, v24, v25
	v_mul_f32_e32 v34, 0x3fb8aa3b, v34
	v_exp_f32_e32 v34, v34
	v_lshl_add_u32 v54, v215, 2, 0
	v_add_u32_e32 v55, 0x1c400, v54
	ds_write_b32 v55, v25
	v_add_u32_e32 v25, 0x1c600, v54
	ds_write_b32 v25, v94
	v_add_u32_e32 v25, 0x1c700, v54
	v_cmp_eq_u32_e32 vcc, 0, v215
	ds_write_b32 v25, v34
	s_and_saveexec_b64 s[0:1], vcc
	s_cbranch_execz .LBB0_232
	s_lshl_b64 s[2:3], s[76:77], 2
	v_readlane_b32 s20, v253, 25
	s_add_u32 s2, s20, s2
	v_readlane_b32 s20, v253, 26
	s_addc_u32 s3, s20, s3
	global_store_dword v141, v24, s[2:3]

.LBB0_233:
	v_lshlrev_b32_e32 v68, 16, v39
	v_and_b32_e32 v69, 0xffff0000, v39
	v_lshlrev_b32_e32 v74, 16, v42
	v_and_b32_e32 v75, 0xffff0000, v42
	v_xor_b32_e32 v39, 32, v209
	v_add_u32_e32 v42, 64, v100
	v_cmp_lt_i32_e32 vcc, v39, v42
	v_lshlrev_b32_e32 v108, 16, v28
	v_and_b32_e32 v109, 0xffff0000, v28
	v_cndmask_b32_e32 v39, v209, v39, vcc
	v_lshlrev_b32_e32 v105, 2, v39
	v_xor_b32_e32 v39, 16, v209
	v_cmp_lt_i32_e32 vcc, v39, v42
	v_lshlrev_b32_e32 v85, 16, v41
	v_and_b32_e32 v81, 0xffff0000, v41
	v_cndmask_b32_e32 v39, v209, v39, vcc
	v_lshlrev_b32_e32 v103, 2, v39
	v_xor_b32_e32 v39, 8, v209
	v_cmp_lt_i32_e32 vcc, v39, v42
	v_lshlrev_b32_e32 v78, 16, v40
	v_and_b32_e32 v79, 0xffff0000, v40
	v_cndmask_b32_e32 v39, v209, v39, vcc
	v_lshlrev_b32_e32 v102, 2, v39
	v_xor_b32_e32 v39, 4, v209
	v_cmp_lt_i32_e32 vcc, v39, v42
	v_lshlrev_b32_e32 v40, 16, v97
	v_and_b32_e32 v41, 0xffff0000, v97
	v_cndmask_b32_e32 v39, v209, v39, vcc
	v_lshlrev_b32_e32 v101, 2, v39
	v_xor_b32_e32 v39, 2, v209
	v_cmp_lt_i32_e32 vcc, v39, v42
	v_lshl_add_u32 v97, v38, 1, 0
	v_bitop3_b32 v38, v215, s82, 7 bitop3:0x6c
	v_cndmask_b32_e32 v39, v209, v39, vcc
	v_lshlrev_b32_e32 v100, 2, v39
	v_xor_b32_e32 v39, 1, v209
	v_cmp_lt_i32_e32 vcc, v39, v42
	v_lshlrev_b32_e32 v116, 16, v32
	v_and_b32_e32 v117, 0xffff0000, v32
	v_cndmask_b32_e32 v39, v209, v39, vcc
	v_lshlrev_b32_e32 v84, 16, v36
	v_and_b32_e32 v91, 0xffff0000, v36
	v_lshlrev_b32_e32 v58, 16, v35
	v_and_b32_e32 v59, 0xffff0000, v35
	v_lshlrev_b32_e32 v66, 16, v37
	v_and_b32_e32 v67, 0xffff0000, v37
	v_lshlrev_b32_e32 v76, 16, v46
	v_and_b32_e32 v77, 0xffff0000, v46
	v_lshlrev_b32_e32 v54, 16, v47
	v_and_b32_e32 v55, 0xffff0000, v47
	v_lshlrev_b32_e32 v46, 16, v52
	v_and_b32_e32 v47, 0xffff0000, v52
	v_lshlrev_b32_e32 v34, 16, v53
	v_and_b32_e32 v35, 0xffff0000, v53
	v_lshlrev_b32_e32 v36, 16, v92
	v_and_b32_e32 v37, 0xffff0000, v92
	v_lshlrev_b32_e32 v52, 16, v98
	v_and_b32_e32 v53, 0xffff0000, v98
	v_lshlrev_b32_e32 v98, 2, v39
	v_lshlrev_b32_e32 v92, 3, v38
	v_pk_fma_f32 v[38:39], v[16:17], v[108:109], 0 op_sel_hi:[1,1,0]
	v_lshlrev_b32_e32 v62, 16, v30
	v_and_b32_e32 v63, 0xffff0000, v30
	v_pk_fma_f32 v[38:39], v[18:19], v[116:117], v[38:39]
	v_lshlrev_b32_e32 v106, 16, v27
	v_pk_fma_f32 v[38:39], v[20:21], v[62:63], v[38:39]
	v_and_b32_e32 v107, 0xffff0000, v27
	v_pk_fma_f32 v[38:39], v[22:23], v[68:69], v[38:39]
	v_lshlrev_b32_e32 v87, 16, v43
	v_and_b32_e32 v83, 0xffff0000, v43
	v_mul_f32_e32 v42, 0xbfb8aa3b, v38
	v_mul_f32_e32 v43, 0xbfb8aa3b, v39
	v_lshlrev_b32_e32 v114, 16, v31
	v_and_b32_e32 v115, 0xffff0000, v31
	v_lshlrev_b32_e32 v72, 16, v44
	v_and_b32_e32 v73, 0xffff0000, v44
	v_lshlrev_b32_e32 v70, 16, v45
	v_and_b32_e32 v64, 0xffff0000, v45
	v_exp_f32_e32 v42, v42
	v_exp_f32_e32 v43, v43
	v_pk_fma_f32 v[44:45], v[8:9], v[106:107], 0 op_sel_hi:[1,1,0]
	v_lshlrev_b32_e32 v112, 16, v29
	v_pk_fma_f32 v[44:45], v[10:11], v[114:115], v[44:45]
	v_and_b32_e32 v88, 0xffff0000, v29
	v_pk_fma_f32 v[44:45], v[12:13], v[58:59], v[44:45]
	v_lshlrev_b32_e32 v71, 16, v49
	v_pk_fma_f32 v[44:45], v[14:15], v[66:67], v[44:45]
	v_and_b32_e32 v65, 0xffff0000, v49
	v_lshlrev_b32_e32 v60, 16, v48
	v_and_b32_e32 v61, 0xffff0000, v48
	v_lshlrev_b32_e32 v29, 16, v57
	v_and_b32_e32 v25, 0xffff0000, v57
	v_lshlrev_b32_e32 v48, 16, v56
	v_and_b32_e32 v49, 0xffff0000, v56
	v_add_f32_e32 v42, 1.0, v42
	v_add_f32_e32 v43, 1.0, v43
	v_mul_f32_e32 v56, 0xbfb8aa3b, v44
	v_mul_f32_e32 v57, 0xbfb8aa3b, v45
	v_rcp_f32_e32 v42, v42
	v_rcp_f32_e32 v43, v43
	v_exp_f32_e32 v56, v56
	v_exp_f32_e32 v57, v57
	v_lshlrev_b32_e32 v113, 16, v33
	v_pk_mul_f32 v[38:39], v[38:39], v[42:43]
	v_add_f32_e32 v42, 1.0, v56
	v_add_f32_e32 v43, 1.0, v57
	v_rcp_f32_e32 v42, v42
	v_rcp_f32_e32 v43, v43
	v_pk_mul_f32 v[56:57], v[38:39], v[38:39]
	v_mov_b32_e32 v86, v85
	v_add_f32_e32 v119, v56, v57
	v_pk_mul_f32 v[44:45], v[44:45], v[42:43]
	v_pk_fma_f32 v[42:43], v[16:17], v[116:117], 0 op_sel_hi:[1,1,0]
	s_waitcnt lgkmcnt(0)
	v_mul_f32_e32 v24, 0xbfb8aa3b, v26
	v_pk_fma_f32 v[42:43], v[18:19], v[62:63], v[42:43]
	v_exp_f32_e32 v24, v24
	v_pk_fma_f32 v[42:43], v[20:21], v[68:69], v[42:43]
	v_and_b32_e32 v89, 0xffff0000, v33
	v_pk_fma_f32 v[42:43], v[22:23], v[74:75], v[42:43]
	v_add_f32_e32 v24, 1.0, v24
	v_mul_f32_e32 v56, 0xbfb8aa3b, v42
	v_exp_f32_e32 v106, v56
	v_mul_f32_e32 v56, 0xbfb8aa3b, v43
	v_exp_f32_e32 v107, v56
	v_pk_mul_f32 v[56:57], v[44:45], v[44:45]
	v_add_f32_e32 v106, 1.0, v106
	v_rcp_f32_e32 v106, v106
	v_add_f32_e32 v107, 1.0, v107
	v_rcp_f32_e32 v107, v107
	v_add_f32_e32 v116, v56, v57
	v_rcp_f32_e32 v95, v24
	v_mov_b32_e32 v90, v89
	v_pk_mul_f32 v[42:43], v[42:43], v[106:107]
	v_pk_fma_f32 v[88:89], v[0:1], v[88:89], 0 op_sel:[1,0,0] op_sel_hi:[1,1,0]
	v_pk_mul_f32 v[56:57], v[42:43], v[42:43]
	v_mov_b32_e32 v80, v91
	v_add_f32_e32 v117, v56, v57
	v_pk_fma_f32 v[56:57], v[8:9], v[114:115], 0 op_sel_hi:[1,1,0]
	v_mov_b32_e32 v114, v113
	v_pk_fma_f32 v[56:57], v[10:11], v[58:59], v[56:57]
	v_mov_b32_e32 v115, v84
	v_pk_fma_f32 v[56:57], v[12:13], v[66:67], v[56:57]
	v_pk_fma_f32 v[112:113], v[0:1], v[112:113], 0 op_sel_hi:[0,1,0]
	v_pk_fma_f32 v[56:57], v[14:15], v[78:79], v[56:57]
	v_pk_fma_f32 v[112:113], v[2:3], v[114:115], v[112:113] op_sel_hi:[0,1,1]
	v_mul_f32_e32 v106, 0xbfb8aa3b, v56
	v_exp_f32_e32 v107, v106
	v_mul_f32_e32 v106, 0xbfb8aa3b, v57
	v_exp_f32_e32 v109, v106
	v_pk_fma_f32 v[112:113], v[4:5], v[84:85], v[112:113] op_sel_hi:[0,1,1]
	v_add_f32_e32 v107, 1.0, v107
	v_pk_fma_f32 v[112:113], v[6:7], v[86:87], v[112:113] op_sel_hi:[0,1,1]
	v_rcp_f32_e32 v108, v107
	v_add_f32_e32 v107, 1.0, v109
	v_mul_f32_e32 v109, 0xbfb8aa3b, v112
	v_exp_f32_e32 v110, v109
	v_mul_f32_e32 v109, 0xbfb8aa3b, v113
	v_exp_f32_e32 v115, v109
	v_rcp_f32_e32 v109, v107
	v_add_f32_e32 v107, 1.0, v110
	v_rcp_f32_e32 v114, v107
	v_add_f32_e32 v107, 1.0, v115
	v_rcp_f32_e32 v115, v107
	v_pk_mul_f32 v[56:57], v[56:57], v[108:109]
	v_readlane_b32 s2, v95, s95
	v_pk_mul_f32 v[108:109], v[56:57], v[56:57]
	v_readlane_b32 s3, v95, s54
	v_add_f32_e32 v120, v108, v109
	v_pk_mul_f32 v[108:109], v[112:113], v[114:115]
	v_pk_fma_f32 v[88:89], v[2:3], v[90:91], v[88:89] op_sel:[1,0,0]
	v_mov_b32_e32 v82, v81
	v_pk_mul_f32 v[108:109], v[108:109], s[2:3]
	v_pk_fma_f32 v[88:89], v[4:5], v[80:81], v[88:89] op_sel:[1,0,0]
	v_cvt_pk_bf16_f32 v107, v108, v109
	v_pk_fma_f32 v[108:109], v[6:7], v[82:83], v[88:89] op_sel:[1,0,0]
	v_pk_fma_f32 v[62:63], v[16:17], v[62:63], 0 op_sel_hi:[1,1,0]
	v_mul_f32_e32 v88, 0xbfb8aa3b, v108
	v_exp_f32_e32 v88, v88
	v_mul_f32_e32 v89, 0xbfb8aa3b, v109
	v_exp_f32_e32 v89, v89
	v_pk_fma_f32 v[62:63], v[18:19], v[68:69], v[62:63]
	v_lshlrev_b32_e32 v32, 16, v50
	v_and_b32_e32 v33, 0xffff0000, v50
	v_lshlrev_b32_e32 v28, 16, v51
	v_and_b32_e32 v24, 0xffff0000, v51
	v_lshlrev_b32_e32 v50, 16, v93
	v_and_b32_e32 v51, 0xffff0000, v93
	v_mul_lo_u32 v93, v215, s11
	v_add_f32_e32 v88, 1.0, v88
	v_pk_fma_f32 v[62:63], v[20:21], v[74:75], v[62:63]
	v_add_lshl_u32 v90, v92, v93, 1
	v_rcp_f32_e32 v112, v88
	v_add_f32_e32 v88, 1.0, v89
	v_pk_fma_f32 v[62:63], v[22:23], v[76:77], v[62:63]
	v_rcp_f32_e32 v113, v88
	v_add_u32_e32 v88, 0, v90
	v_add_u32_e32 v91, s12, v90
	v_mul_f32_e32 v90, 0xbfb8aa3b, v62
	v_exp_f32_e32 v90, v90
	v_mul_f32_e32 v110, 0xbfb8aa3b, v63
	v_exp_f32_e32 v110, v110
	v_pk_fma_f32 v[58:59], v[8:9], v[58:59], 0 op_sel_hi:[1,1,0]
	v_add_f32_e32 v90, 1.0, v90
	v_pk_fma_f32 v[58:59], v[10:11], v[66:67], v[58:59]
	v_pk_mul_f32 v[108:109], v[108:109], v[112:113]
	v_pk_fma_f32 v[58:59], v[12:13], v[78:79], v[58:59]
	v_rcp_f32_e32 v112, v90
	v_pk_fma_f32 v[114:115], v[14:15], v[72:73], v[58:59]
	v_add_f32_e32 v90, 1.0, v110
	v_mul_f32_e32 v58, 0xbfb8aa3b, v114
	v_rcp_f32_e32 v113, v90
	v_exp_f32_e32 v90, v58
	v_mul_f32_e32 v58, 0xbfb8aa3b, v115
	v_exp_f32_e32 v110, v58
	v_pk_mul_f32 v[58:59], v[62:63], v[112:113]
	v_add_f32_e32 v62, 1.0, v90
	v_rcp_f32_e32 v62, v62
	v_add_f32_e32 v63, 1.0, v110
	v_rcp_f32_e32 v63, v63
	v_pk_fma_f32 v[68:69], v[16:17], v[68:69], 0 op_sel_hi:[1,1,0]
	v_pk_mul_f32 v[112:113], v[58:59], v[58:59]
	v_pk_fma_f32 v[68:69], v[18:19], v[74:75], v[68:69]
	v_pk_mul_f32 v[62:63], v[114:115], v[62:63]
	v_pk_fma_f32 v[68:69], v[20:21], v[76:77], v[68:69]
	v_add_f32_e32 v122, v112, v113
	v_pk_fma_f32 v[68:69], v[22:23], v[60:61], v[68:69]
	v_pk_mul_f32 v[112:113], v[62:63], v[62:63]
	v_mul_f32_e32 v110, 0xbfb8aa3b, v68
	v_add_f32_e32 v123, v112, v113
	v_exp_f32_e32 v110, v110
	v_mul_f32_e32 v112, 0xbfb8aa3b, v69
	v_exp_f32_e32 v113, v112
	v_pk_fma_f32 v[66:67], v[8:9], v[66:67], 0 op_sel_hi:[1,1,0]
	v_add_f32_e32 v110, 1.0, v110
	v_pk_fma_f32 v[66:67], v[10:11], v[78:79], v[66:67]
	v_rcp_f32_e32 v112, v110
	v_pk_fma_f32 v[66:67], v[12:13], v[72:73], v[66:67]
	v_add_f32_e32 v110, 1.0, v113
	v_pk_fma_f32 v[114:115], v[14:15], v[54:55], v[66:67]
	v_rcp_f32_e32 v113, v110
	v_mul_f32_e32 v66, 0xbfb8aa3b, v114
	v_exp_f32_e32 v110, v66
	v_mul_f32_e32 v66, 0xbfb8aa3b, v115
	v_exp_f32_e32 v124, v66
	v_pk_mul_f32 v[66:67], v[68:69], v[112:113]
	v_add_f32_e32 v68, 1.0, v110
	v_pk_mul_f32 v[112:113], v[66:67], v[66:67]
	v_add_f32_e32 v69, 1.0, v124
	v_pk_fma_f32 v[84:85], v[0:1], v[84:85], 0 op_sel_hi:[0,1,0]
	v_rcp_f32_e32 v68, v68
	v_rcp_f32_e32 v69, v69
	v_add_f32_e32 v124, v112, v113
	v_pk_mov_b32 v[112:113], v[86:87], v[70:71] op_sel:[1,0]
	v_pk_fma_f32 v[84:85], v[2:3], v[86:87], v[84:85] op_sel_hi:[0,1,1]
	v_pk_fma_f32 v[84:85], v[4:5], v[112:113], v[84:85] op_sel_hi:[0,1,1]
	v_pk_fma_f32 v[84:85], v[6:7], v[70:71], v[84:85] op_sel_hi:[0,1,1]
	v_mul_f32_e32 v86, 0xbfb8aa3b, v84
	v_pk_mul_f32 v[68:69], v[114:115], v[68:69]
	v_exp_f32_e32 v114, v86
	v_mul_f32_e32 v86, 0xbfb8aa3b, v85
	v_exp_f32_e32 v115, v86
	v_pk_mul_f32 v[86:87], v[68:69], v[68:69]
	v_add_f32_e32 v114, 1.0, v114
	v_pk_fma_f32 v[80:81], v[0:1], v[80:81], 0 op_sel:[1,0,0] op_sel_hi:[1,1,0]
	v_add_f32_e32 v115, 1.0, v115
	v_rcp_f32_e32 v114, v114
	v_rcp_f32_e32 v115, v115
	v_add_f32_e32 v125, v86, v87
	v_pk_mov_b32 v[86:87], v[82:83], v[64:65] op_sel:[1,0]
	v_pk_fma_f32 v[80:81], v[2:3], v[82:83], v[80:81] op_sel:[1,0,0]
	v_pk_mul_f32 v[84:85], v[84:85], v[114:115]
	v_pk_fma_f32 v[80:81], v[4:5], v[86:87], v[80:81] op_sel:[1,0,0]
	s_mul_i32 s1, s76, 0x12000
	v_pk_fma_f32 v[80:81], v[6:7], v[64:65], v[80:81] op_sel:[1,0,0]
	s_mul_hi_i32 s0, s76, 0x12000
	v_mul_f32_e32 v82, 0xbfb8aa3b, v80
	v_exp_f32_e32 v114, v82
	v_mul_f32_e32 v82, 0xbfb8aa3b, v81
	v_exp_f32_e32 v115, v82
	s_add_u32 s78, s40, s1
	s_addc_u32 s79, s41, s0
	s_mul_i32 s0, s82, 0x440
	v_readlane_b32 s82, v95, s55
	v_readlane_b32 s83, v95, s33
	v_pk_fma_f32 v[74:75], v[16:17], v[74:75], 0 op_sel_hi:[1,1,0]
	v_pk_fma_f32 v[78:79], v[8:9], v[78:79], 0 op_sel_hi:[1,1,0]
	v_pk_mul_f32 v[82:83], v[84:85], s[82:83]
	v_add_f32_e32 v84, 1.0, v114
	v_rcp_f32_e32 v114, v84
	v_add_f32_e32 v84, 1.0, v115
	v_rcp_f32_e32 v115, v84
	v_pk_fma_f32 v[74:75], v[18:19], v[76:77], v[74:75]
	v_cvt_pk_bf16_f32 v84, v82, v83
	v_pk_fma_f32 v[74:75], v[20:21], v[60:61], v[74:75]
	v_pk_mul_f32 v[80:81], v[80:81], v[114:115]
	v_pk_fma_f32 v[74:75], v[22:23], v[46:47], v[74:75]
	v_pk_mul_f32 v[80:81], v[80:81], s[82:83]
	v_mul_f32_e32 v82, 0xbfb8aa3b, v74
	v_mul_f32_e32 v114, 0xbfb8aa3b, v75
	v_exp_f32_e32 v82, v82
	v_exp_f32_e32 v114, v114
	v_cvt_pk_bf16_f32 v115, v80, v81
	v_pk_fma_f32 v[78:79], v[10:11], v[72:73], v[78:79]
	v_add_f32_e32 v80, 1.0, v82
	v_add_f32_e32 v81, 1.0, v114
	v_rcp_f32_e32 v80, v80
	v_rcp_f32_e32 v81, v81
	v_pk_fma_f32 v[78:79], v[12:13], v[54:55], v[78:79]
	v_and_b32_e32 v118, 32, v215
	v_pk_fma_f32 v[78:79], v[14:15], v[32:33], v[78:79]
	v_pk_mul_f32 v[74:75], v[74:75], v[80:81]
	v_cmp_eq_u32_e32 vcc, 0, v118
	v_pk_mul_f32 v[80:81], v[74:75], v[74:75]
	v_mul_f32_e32 v118, 0xbfb8aa3b, v79
	v_add_f32_e32 v80, v80, v81
	v_mul_f32_e32 v81, 0xbfb8aa3b, v78
	v_exp_f32_e32 v81, v81
	v_exp_f32_e32 v118, v118
	v_add_u32_e32 v89, 0x48, v93
	v_or_b32_e32 v126, 2, v92
	v_add_u32_e32 v83, v126, v89
	v_lshl_add_u32 v114, v83, 1, s12
	v_cndmask_b32_e32 v83, v80, v119, vcc
	v_cndmask_b32_e32 v80, v119, v80, vcc
	ds_bpermute_b32 v119, v105, v80
	v_add_f32_e32 v80, 1.0, v81
	v_add_f32_e32 v81, 1.0, v118
	v_rcp_f32_e32 v80, v80
	v_rcp_f32_e32 v81, v81
	v_pk_fma_f32 v[76:77], v[16:17], v[76:77], 0 op_sel_hi:[1,1,0]
	s_waitcnt lgkmcnt(0)
	v_add_f32_e32 v118, v83, v119
	v_pk_fma_f32 v[76:77], v[18:19], v[60:61], v[76:77]
	v_pk_mul_f32 v[78:79], v[78:79], v[80:81]
	v_pk_fma_f32 v[76:77], v[20:21], v[46:47], v[76:77]
	v_pk_mul_f32 v[80:81], v[78:79], v[78:79]
	v_pk_fma_f32 v[76:77], v[22:23], v[48:49], v[76:77]
	v_add_f32_e32 v80, v80, v81
	v_cndmask_b32_e32 v119, v80, v116, vcc
	v_cndmask_b32_e32 v80, v116, v80, vcc
	v_mul_f32_e32 v81, 0xbfb8aa3b, v76
	v_mul_f32_e32 v116, 0xbfb8aa3b, v77
	v_exp_f32_e32 v81, v81
	v_exp_f32_e32 v116, v116
	v_pk_mul_f32 v[108:109], v[108:109], s[2:3]
	v_add_lshl_u32 v121, v92, v89, 1
	v_cvt_pk_bf16_f32 v108, v108, v109
	v_add_u32_e32 v109, s12, v121
	v_add_u32_e32 v82, 0, v121
	ds_bpermute_b32 v121, v105, v80
	v_add_f32_e32 v80, 1.0, v81
	v_add_f32_e32 v81, 1.0, v116
	v_rcp_f32_e32 v80, v80
	v_rcp_f32_e32 v81, v81
	v_pk_fma_f32 v[72:73], v[8:9], v[72:73], 0 op_sel_hi:[1,1,0]
	s_waitcnt lgkmcnt(0)
	v_add_f32_e32 v116, v119, v121
	v_pk_fma_f32 v[72:73], v[10:11], v[54:55], v[72:73]
	v_pk_mul_f32 v[76:77], v[76:77], v[80:81]
	v_pk_fma_f32 v[72:73], v[12:13], v[32:33], v[72:73]
	v_pk_mul_f32 v[80:81], v[76:77], v[76:77]
	v_pk_fma_f32 v[72:73], v[14:15], v[34:35], v[72:73]
	v_add_f32_e32 v119, v80, v81
	v_mul_f32_e32 v81, 0xbfb8aa3b, v72
	v_mul_f32_e32 v121, 0xbfb8aa3b, v73
	v_exp_f32_e32 v81, v81
	v_exp_f32_e32 v121, v121
	v_cndmask_b32_e32 v80, v117, v119, vcc
	v_add_u32_e32 v127, v126, v93
	ds_bpermute_b32 v126, v105, v80
	v_add_f32_e32 v80, 1.0, v81
	v_add_f32_e32 v81, 1.0, v121
	v_rcp_f32_e32 v80, v80
	v_rcp_f32_e32 v81, v81
	v_pk_fma_f32 v[112:113], v[0:1], v[112:113], 0 op_sel_hi:[0,1,0]
	v_cndmask_b32_e32 v117, v119, v117, vcc
	s_waitcnt lgkmcnt(0)
	v_add_f32_e32 v117, v117, v126
	v_pk_mul_f32 v[80:81], v[72:73], v[80:81]
	v_pk_fma_f32 v[60:61], v[16:17], v[60:61], 0 op_sel_hi:[1,1,0]
	v_pk_mul_f32 v[72:73], v[80:81], v[80:81]
	v_pk_fma_f32 v[60:61], v[18:19], v[46:47], v[60:61]
	v_add_f32_e32 v72, v72, v73
	v_cndmask_b32_e32 v121, v72, v120, vcc
	v_cndmask_b32_e32 v120, v120, v72, vcc
	v_pk_mov_b32 v[72:73], v[70:71], v[28:29] op_sel:[1,0]
	v_pk_fma_f32 v[70:71], v[2:3], v[70:71], v[112:113] op_sel_hi:[0,1,1]
	v_pk_fma_f32 v[70:71], v[4:5], v[72:73], v[70:71] op_sel_hi:[0,1,1]
	v_pk_fma_f32 v[70:71], v[6:7], v[28:29], v[70:71] op_sel_hi:[0,1,1]
	v_mul_f32_e32 v112, 0xbfb8aa3b, v71
	v_exp_f32_e32 v112, v112
	v_mul_f32_e32 v113, 0xbfb8aa3b, v70
	v_exp_f32_e32 v126, v113
	v_pk_fma_f32 v[60:61], v[20:21], v[48:49], v[60:61]
	v_add_f32_e32 v112, 1.0, v112
	v_rcp_f32_e32 v113, v112
	v_add_f32_e32 v112, 1.0, v126
	v_rcp_f32_e32 v112, v112
	v_readlane_b32 s92, v95, s4
	v_readlane_b32 s93, v95, s5
	v_pk_fma_f32 v[86:87], v[0:1], v[86:87], 0 op_sel:[1,0,0] op_sel_hi:[1,1,0]
	v_pk_mul_f32 v[70:71], v[70:71], v[112:113]
	v_pk_fma_f32 v[60:61], v[22:23], v[50:51], v[60:61]
	v_pk_mul_f32 v[112:113], v[70:71], s[92:93]
	v_pk_mov_b32 v[70:71], v[64:65], v[24:25] op_sel:[1,0]
	v_pk_fma_f32 v[64:65], v[2:3], v[64:65], v[86:87] op_sel:[1,0,0]
	v_mul_f32_e32 v86, 0xbfb8aa3b, v60
	v_mul_f32_e32 v87, 0xbfb8aa3b, v61
	v_exp_f32_e32 v86, v86
	v_exp_f32_e32 v87, v87
	v_pk_fma_f32 v[54:55], v[8:9], v[54:55], 0 op_sel_hi:[1,1,0]
	v_pk_fma_f32 v[16:17], v[16:17], v[46:47], 0 op_sel_hi:[1,1,0]
	v_add_f32_e32 v86, 1.0, v86
	v_add_f32_e32 v87, 1.0, v87
	v_rcp_f32_e32 v86, v86
	v_rcp_f32_e32 v87, v87
	v_pk_fma_f32 v[8:9], v[8:9], v[32:33], 0 op_sel_hi:[1,1,0]
	v_pk_fma_f32 v[54:55], v[10:11], v[32:33], v[54:55]
	v_pk_fma_f32 v[16:17], v[18:19], v[48:49], v[16:17]
	v_pk_mul_f32 v[60:61], v[60:61], v[86:87]
	v_pk_fma_f32 v[8:9], v[10:11], v[34:35], v[8:9]
	v_pk_mul_f32 v[86:87], v[60:61], v[60:61]
	v_pk_fma_f32 v[54:55], v[12:13], v[34:35], v[54:55]
	v_add_f32_e32 v86, v86, v87
	v_pk_fma_f32 v[16:17], v[20:21], v[50:51], v[16:17]
	v_pk_fma_f32 v[8:9], v[12:13], v[36:37], v[8:9]
	v_cndmask_b32_e32 v87, v122, v86, vcc
	v_pk_fma_f32 v[54:55], v[14:15], v[36:37], v[54:55]
	v_pk_fma_f32 v[16:17], v[22:23], v[52:53], v[16:17]
	v_pk_fma_f32 v[8:9], v[14:15], v[40:41], v[8:9]
	v_lshlrev_b32_e32 v30, 16, v96
	v_and_b32_e32 v26, 0xffff0000, v96
	v_lshl_add_u32 v96, s0, 1, v97
	s_mul_i32 s0, s54, 0x88
	ds_bpermute_b32 v128, v105, v87
	v_cvt_pk_bf16_f32 v129, v112, v113
	v_mul_f32_e32 v112, 0xbfb8aa3b, v54
	v_mul_f32_e32 v113, 0xbfb8aa3b, v55
	v_mul_f32_e32 v18, 0xbfb8aa3b, v16
	v_mul_f32_e32 v19, 0xbfb8aa3b, v17
	v_mul_f32_e32 v10, 0xbfb8aa3b, v8
	v_mul_f32_e32 v11, 0xbfb8aa3b, v9
	v_lshl_add_u32 v106, s0, 1, v97
	v_readlane_b32 s0, v253, 45
	v_exp_f32_e32 v112, v112
	v_exp_f32_e32 v113, v113
	v_exp_f32_e32 v18, v18
	v_exp_f32_e32 v19, v19
	v_exp_f32_e32 v10, v10
	v_exp_f32_e32 v11, v11
	v_lshl_add_u32 v90, s0, 1, v97
	v_readlane_b32 s0, v253, 46
	v_and_b32_e32 v111, 16, v215
	v_cndmask_b32_e32 v86, v86, v122, vcc
	v_lshl_add_u32 v110, s0, 1, v97
	v_readlane_b32 s0, v253, 47
	s_waitcnt lgkmcnt(0)
	v_add_f32_e32 v86, v86, v128
	v_add_f32_e32 v112, 1.0, v112
	v_lshl_add_u32 v83, s0, 1, v97
	v_readlane_b32 s0, v253, 48
	v_add_f32_e32 v113, 1.0, v113
	v_add_f32_e32 v18, 1.0, v18
	v_lshl_add_u32 v119, s0, 1, v97
	v_cmp_eq_u32_e64 s[0:1], 0, v111
	v_add_f32_e32 v19, 1.0, v19
	v_add_f32_e32 v10, 1.0, v10
	v_add_f32_e32 v11, 1.0, v11
	v_cndmask_b32_e64 v111, v86, v118, s[0:1]
	v_cndmask_b32_e64 v86, v118, v86, s[0:1]
	v_rcp_f32_e32 v112, v112
	v_rcp_f32_e32 v113, v113
	v_rcp_f32_e32 v18, v18
	v_rcp_f32_e32 v19, v19
	v_rcp_f32_e32 v10, v10
	v_rcp_f32_e32 v11, v11
	ds_bpermute_b32 v86, v103, v86
	v_pk_mul_f32 v[54:55], v[54:55], v[112:113]
	v_pk_mul_f32 v[16:17], v[16:17], v[18:19]
	v_pk_mul_f32 v[8:9], v[8:9], v[10:11]
	v_pk_mul_f32 v[112:113], v[54:55], v[54:55]
	v_pk_mul_f32 v[18:19], v[16:17], v[16:17]
	v_pk_mul_f32 v[10:11], v[8:9], v[8:9]
	s_waitcnt lgkmcnt(0)
	v_add_f32_e32 v86, v111, v86
	v_add_f32_e32 v111, v112, v113
	v_add_f32_e32 v18, v18, v19
	v_add_f32_e32 v10, v10, v11
	v_cndmask_b32_e32 v112, v111, v123, vcc
	v_cndmask_b32_e32 v111, v123, v111, vcc
	v_cndmask_b32_e32 v19, v18, v124, vcc
	v_cndmask_b32_e32 v18, v124, v18, vcc
	v_cndmask_b32_e32 v11, v125, v10, vcc
	ds_bpermute_b32 v120, v105, v120
	ds_bpermute_b32 v111, v105, v111
	ds_bpermute_b32 v12, v105, v18
	ds_bpermute_b32 v11, v105, v11
	v_cndmask_b32_e32 v10, v10, v125, vcc
	s_waitcnt lgkmcnt(3)
	v_add_f32_e32 v120, v121, v120
	s_waitcnt lgkmcnt(2)
	v_add_f32_e32 v20, v112, v111
	s_waitcnt lgkmcnt(1)
	v_add_f32_e32 v12, v19, v12
	s_waitcnt lgkmcnt(0)
	v_add_f32_e32 v10, v10, v11
	v_cndmask_b32_e64 v21, v20, v116, s[0:1]
	v_cndmask_b32_e64 v20, v116, v20, s[0:1]
	v_cndmask_b32_e64 v13, v117, v12, s[0:1]
	v_cndmask_b32_e64 v11, v120, v10, s[0:1]
	ds_bpermute_b32 v20, v103, v20
	ds_bpermute_b32 v13, v103, v13
	ds_bpermute_b32 v11, v103, v11
	v_and_b32_e32 v104, 8, v215
	v_cndmask_b32_e64 v12, v12, v117, s[0:1]
	v_cndmask_b32_e64 v10, v10, v120, s[0:1]
	s_waitcnt lgkmcnt(2)
	v_add_f32_e32 v14, v21, v20
	s_waitcnt lgkmcnt(1)
	v_add_f32_e32 v12, v12, v13
	v_cmp_eq_u32_e32 vcc, 0, v104
	s_waitcnt lgkmcnt(0)
	v_add_f32_e32 v10, v10, v11
	v_lshlrev_b32_e32 v31, 16, v99
	v_cndmask_b32_e32 v13, v12, v86, vcc
	v_cndmask_b32_e32 v12, v86, v12, vcc
	v_cndmask_b32_e32 v11, v14, v10, vcc
	ds_bpermute_b32 v12, v102, v12
	ds_bpermute_b32 v11, v102, v11
	v_and_b32_e32 v27, 0xffff0000, v99
	v_and_b32_e32 v99, 4, v215
	v_pk_fma_f32 v[64:65], v[4:5], v[70:71], v[64:65] op_sel:[1,0,0]
	v_cndmask_b32_e32 v10, v10, v14, vcc
	v_pk_fma_f32 v[64:65], v[6:7], v[24:25], v[64:65] op_sel:[1,0,0]
	s_waitcnt lgkmcnt(1)
	v_add_f32_e32 v12, v13, v12
	s_waitcnt lgkmcnt(0)
	v_add_f32_e32 v10, v10, v11
	v_cmp_eq_u32_e32 vcc, 0, v99
	v_lshl_add_u32 v85, v127, 1, s12
	v_mul_f32_e32 v127, 0xbfb8aa3b, v65
	v_mul_f32_e32 v118, 0xbfb8aa3b, v64
	v_cndmask_b32_e32 v13, v12, v10, vcc
	v_cndmask_b32_e32 v10, v10, v12, vcc
	v_exp_f32_e32 v127, v127
	v_exp_f32_e32 v118, v118
	ds_bpermute_b32 v12, v101, v10
	v_readlane_b32 s0, v253, 49
	v_add_f32_e32 v87, 1.0, v127
	v_add_f32_e32 v15, 1.0, v118
	v_rcp_f32_e32 v87, v87
	v_rcp_f32_e32 v86, v15
	s_waitcnt lgkmcnt(0)
	v_add_f32_e32 v12, v13, v12
	ds_bpermute_b32 v13, v100, v12
	v_lshl_add_u32 v33, s0, 1, v97
	v_pk_mul_f32 v[10:11], v[64:65], v[86:87]
	v_readlane_b32 s0, v253, 50
	v_pk_mul_f32 v[10:11], v[10:11], s[92:93]
	s_mov_b32 s74, 0x358637bd
	v_cvt_pk_bf16_f32 v23, v10, v11
	s_waitcnt lgkmcnt(0)
	v_add_f32_e32 v10, v12, v13
	ds_bpermute_b32 v11, v98, v10
	v_or_b32_e32 v121, 4, v92
	v_lshl_add_u32 v34, s0, 1, v97
	v_add_u32_e32 v14, v121, v89
	v_lshl_add_u32 v32, v14, 1, s12
	s_waitcnt lgkmcnt(0)
	v_add_f32_e32 v35, v10, v11
	v_mov_b64_e32 v[10:11], s[74:75]
	v_readlane_b32 s1, v35, 0
	v_readlane_b32 s0, v35, 4
	v_readlane_b32 s80, v94, s95
	v_readlane_b32 s81, v94, s54
	v_pk_add_f32 v[12:13], s[0:1], v[10:11] op_sel_hi:[1,0]
	v_readlane_b32 s20, v94, s55
	v_readlane_b32 s21, v94, s33
	v_rsq_f32_e32 v13, v13
	v_rsq_f32_e32 v14, v12
	v_mov_b32_e32 v12, v13
	v_mul_f32_e32 v12, 0x3db504f3, v12
	v_pk_mul_f32 v[12:13], v[44:45], v[12:13] op_sel_hi:[1,0]
	v_readlane_b32 s1, v35, 8
	v_cvt_pk_bf16_f32 v12, v12, v13
	v_readlane_b32 s0, v35, 12
	ds_write_b32 v96, v12 offset:34816
	v_pk_mul_f32 v[14:15], v[38:39], v[14:15] op_sel_hi:[1,0]
	v_pk_add_f32 v[12:13], s[0:1], v[10:11] op_sel_hi:[1,0]
	v_cvt_pk_bf16_f32 v36, v14, v15
	v_readlane_b32 s22, v94, s4
	v_rsq_f32_e32 v13, v13
	v_rsq_f32_e32 v18, v12
	v_mov_b32_e32 v12, v13
	v_mul_f32_e32 v12, 0x3db504f3, v12
	v_pk_mul_f32 v[12:13], v[56:57], v[12:13] op_sel_hi:[1,0]
	v_pk_mul_f32 v[18:19], v[42:43], v[18:19] op_sel_hi:[1,0]
	v_cvt_pk_bf16_f32 v12, v12, v13
	v_cvt_pk_bf16_f32 v37, v18, v19
	ds_write_b32 v106, v12 offset:34816
	v_mov_b32_e32 v12, v14
	v_mov_b32_e32 v13, v18
	v_mov_b32_e32 v18, v15
	v_pk_mul_f32 v[12:13], s[2:3], v[12:13]
	v_pk_mul_f32 v[14:15], s[2:3], v[18:19]
	v_pk_mul_f32 v[20:21], s[80:81], v[12:13]
	v_cvt_pk_bf16_f32 v12, v12, v14
	v_pk_mul_f32 v[18:19], s[80:81], v[14:15]
	ds_write2st64_b32 v96, v36, v12 offset1:68
	v_cvt_pk_bf16_f32 v12, v13, v15
	v_cvt_pk_bf16_f32 v20, v20, v21
	ds_write2st64_b32 v106, v37, v12 offset1:68
	ds_write_b32 v88, v107 offset:52224
	ds_write_b32 v91, v20
	ds_write_b32 v88, v108 offset:52368
	v_cvt_pk_bf16_f32 v12, v18, v19
	v_readlane_b32 s1, v35, 16
	v_readlane_b32 s0, v35, 20
	ds_write_b32 v109, v12
	v_readlane_b32 s23, v94, s5
	v_pk_add_f32 v[12:13], s[0:1], v[10:11] op_sel_hi:[1,0]
	v_add_u32_e32 v126, v121, v93
	v_lshl_add_u32 v22, v126, 1, s12
	v_rsq_f32_e32 v13, v13
	v_rsq_f32_e32 v14, v12
	v_mov_b32_e32 v12, v13
	v_mul_f32_e32 v12, 0x3db504f3, v12
	v_pk_mul_f32 v[12:13], v[62:63], v[12:13] op_sel_hi:[1,0]
	v_readlane_b32 s1, v35, 24
	v_cvt_pk_bf16_f32 v12, v12, v13
	v_readlane_b32 s0, v35, 28
	ds_write_b32 v90, v12 offset:34816
	v_pk_mul_f32 v[14:15], v[58:59], v[14:15] op_sel_hi:[1,0]
	v_pk_add_f32 v[12:13], s[0:1], v[10:11] op_sel_hi:[1,0]
	v_cvt_pk_bf16_f32 v36, v14, v15
	v_readlane_b32 s96, v95, s6
	v_rsq_f32_e32 v13, v13
	v_rsq_f32_e32 v18, v12
	v_mov_b32_e32 v12, v13
	v_mul_f32_e32 v12, 0x3db504f3, v12
	v_pk_mul_f32 v[12:13], v[68:69], v[12:13] op_sel_hi:[1,0]
	v_pk_mul_f32 v[18:19], v[66:67], v[18:19] op_sel_hi:[1,0]
	v_cvt_pk_bf16_f32 v12, v12, v13
	v_cvt_pk_bf16_f32 v37, v18, v19
	ds_write_b32 v110, v12 offset:34816
	v_mov_b32_e32 v12, v14
	v_mov_b32_e32 v13, v18
	v_mov_b32_e32 v18, v15
	v_pk_mul_f32 v[12:13], s[82:83], v[12:13]
	v_pk_mul_f32 v[14:15], s[82:83], v[18:19]
	v_pk_mul_f32 v[20:21], s[20:21], v[12:13]
	v_cvt_pk_bf16_f32 v12, v12, v14
	v_pk_mul_f32 v[18:19], s[20:21], v[14:15]
	ds_write2st64_b32 v90, v36, v12 offset1:68
	v_cvt_pk_bf16_f32 v12, v13, v15
	v_cvt_pk_bf16_f32 v20, v20, v21
	ds_write2st64_b32 v110, v37, v12 offset1:68
	ds_write_b32 v88, v84 offset:52228
	ds_write_b32 v85, v20
	ds_write_b32 v82, v115 offset:52228
	v_cvt_pk_bf16_f32 v12, v18, v19
	v_readlane_b32 s1, v35, 32
	v_readlane_b32 s0, v35, 36
	ds_write_b32 v114, v12
	v_readlane_b32 s97, v95, s7
	v_pk_add_f32 v[12:13], s[0:1], v[10:11] op_sel_hi:[1,0]
	v_readlane_b32 s34, v94, s6
	v_readlane_b32 s35, v94, s7
	v_rsq_f32_e32 v13, v13
	v_rsq_f32_e32 v14, v12
	v_mov_b32_e32 v12, v13
	v_mul_f32_e32 v12, 0x3db504f3, v12
	v_pk_mul_f32 v[12:13], v[78:79], v[12:13] op_sel_hi:[1,0]
	v_pk_mul_f32 v[14:15], v[74:75], v[14:15] op_sel_hi:[1,0]
	v_cvt_pk_bf16_f32 v12, v12, v13
	v_readlane_b32 s1, v35, 40
	v_readlane_b32 s0, v35, 44
	v_cvt_pk_bf16_f32 v18, v14, v15
	ds_write_b32 v83, v12 offset:34816
	v_pk_add_f32 v[12:13], s[0:1], v[10:11] op_sel_hi:[1,0]
	ds_write_b32 v83, v18
	s_mov_b64 s[2:3], -1
	v_rsq_f32_e32 v13, v13
	v_rsq_f32_e32 v18, v12
	v_mov_b32_e32 v12, v13
	v_mul_f32_e32 v12, 0x3db504f3, v12
	v_pk_mul_f32 v[12:13], v[80:81], v[12:13] op_sel_hi:[1,0]
	v_pk_mul_f32 v[18:19], v[76:77], v[18:19] op_sel_hi:[1,0]
	v_cvt_pk_bf16_f32 v12, v12, v13
	v_cvt_pk_bf16_f32 v20, v18, v19
	ds_write_b32 v119, v12 offset:34816
	v_mov_b32_e32 v12, v14
	v_mov_b32_e32 v13, v18
	v_mov_b32_e32 v18, v15
	v_pk_mul_f32 v[12:13], s[92:93], v[12:13]
	v_pk_mul_f32 v[14:15], s[92:93], v[18:19]
	ds_write_b32 v119, v20
	v_pk_mul_f32 v[20:21], s[22:23], v[12:13]
	v_cvt_pk_bf16_f32 v12, v12, v14
	v_pk_mul_f32 v[18:19], s[22:23], v[14:15]
	ds_write_b32 v83, v12 offset:17408
	v_cvt_pk_bf16_f32 v12, v13, v15
	v_cvt_pk_bf16_f32 v20, v20, v21
	ds_write_b32 v119, v12 offset:17408
	ds_write_b32 v88, v129 offset:52232
	ds_write_b32 v22, v20
	ds_write_b32 v82, v23 offset:52232
	v_cvt_pk_bf16_f32 v12, v18, v19
	v_readlane_b32 s1, v35, 48
	v_readlane_b32 s0, v35, 52
	ds_write_b32 v32, v12
	s_nop 0
	v_pk_add_f32 v[12:13], s[0:1], v[10:11] op_sel_hi:[1,0]
	s_nop 0
	s_nop 0
	v_rsq_f32_e32 v13, v13
	v_rsq_f32_e32 v14, v12
	v_mov_b32_e32 v12, v13
	v_mul_f32_e32 v12, 0x3db504f3, v12
	v_pk_mul_f32 v[12:13], v[54:55], v[12:13] op_sel_hi:[1,0]
	v_readlane_b32 s1, v35, 56
	v_readlane_b32 s0, v35, 60
	v_cvt_pk_bf16_f32 v12, v12, v13
	ds_write_b32 v33, v12 offset:34816
	v_pk_add_f32 v[10:11], s[0:1], v[10:11] op_sel_hi:[1,0]
	v_pk_mul_f32 v[14:15], v[60:61], v[14:15] op_sel_hi:[1,0]
	v_cvt_pk_bf16_f32 v18, v14, v15
	v_rsq_f32_e32 v11, v11
	v_rsq_f32_e32 v12, v10
	ds_write_b32 v33, v18
	v_mov_b32_e32 v10, v11
	v_mul_f32_e32 v10, 0x3db504f3, v10
	v_pk_mul_f32 v[8:9], v[8:9], v[10:11] op_sel_hi:[1,0]
	v_pk_mul_f32 v[10:11], v[16:17], v[12:13] op_sel_hi:[1,0]
	v_pk_fma_f32 v[16:17], v[0:1], v[72:73], 0 op_sel_hi:[0,1,0]
	v_cvt_pk_bf16_f32 v12, v10, v11
	ds_write_b32 v34, v12
	v_pk_mov_b32 v[12:13], v[28:29], v[30:31] op_sel:[1,0]
	v_pk_fma_f32 v[16:17], v[2:3], v[28:29], v[16:17] op_sel_hi:[0,1,1]
	v_pk_fma_f32 v[12:13], v[4:5], v[12:13], v[16:17] op_sel_hi:[0,1,1]
	v_pk_fma_f32 v[12:13], v[6:7], v[30:31], v[12:13] op_sel_hi:[0,1,1]
	v_mul_f32_e32 v16, 0xbfb8aa3b, v13
	v_exp_f32_e32 v16, v16
	v_mul_f32_e32 v17, 0xbfb8aa3b, v12
	v_exp_f32_e32 v17, v17
	v_cvt_pk_bf16_f32 v18, v8, v9
	v_add_f32_e32 v8, 1.0, v16
	v_rcp_f32_e32 v9, v8
	v_add_f32_e32 v8, 1.0, v17
	v_rcp_f32_e32 v8, v8
	v_pk_fma_f32 v[0:1], v[0:1], v[70:71], 0 op_sel:[1,0,0] op_sel_hi:[1,1,0]
	ds_write_b32 v34, v18 offset:34816
	v_pk_fma_f32 v[0:1], v[2:3], v[24:25], v[0:1] op_sel:[1,0,0]
	v_pk_mul_f32 v[8:9], v[12:13], v[8:9]
	v_pk_mov_b32 v[12:13], v[24:25], v[26:27] op_sel:[1,0]
	v_pk_mul_f32 v[8:9], v[8:9], s[96:97]
	v_pk_fma_f32 v[0:1], v[4:5], v[12:13], v[0:1] op_sel:[1,0,0]
	v_cvt_pk_bf16_f32 v18, v8, v9
	v_pk_fma_f32 v[0:1], v[6:7], v[26:27], v[0:1] op_sel:[1,0,0]
	v_mov_b32_e32 v8, v14
	v_mul_f32_e32 v2, 0xbfb8aa3b, v1
	v_exp_f32_e32 v4, v2
	v_mul_f32_e32 v2, 0xbfb8aa3b, v0
	v_exp_f32_e32 v6, v2
	v_mov_b32_e32 v9, v10
	v_add_f32_e32 v4, 1.0, v4
	v_rcp_f32_e32 v5, v4
	v_add_f32_e32 v4, 1.0, v6
	v_rcp_f32_e32 v4, v4
	v_pk_mul_f32 v[8:9], s[96:97], v[8:9]
	v_mov_b32_e32 v10, v15
	v_pk_mul_f32 v[2:3], s[34:35], v[8:9]
	v_pk_mul_f32 v[0:1], v[0:1], v[4:5]
	v_or_b32_e32 v16, 6, v92
	v_pk_mul_f32 v[0:1], v[0:1], s[96:97]
	v_cvt_pk_bf16_f32 v6, v2, v3
	v_cvt_pk_bf16_f32 v4, v0, v1
	v_pk_mul_f32 v[0:1], s[96:97], v[10:11]
	v_add_u32_e32 v17, v16, v93
	v_pk_mul_f32 v[2:3], s[34:35], v[0:1]
	v_cvt_pk_bf16_f32 v0, v8, v0
	v_add_u32_e32 v12, v16, v89
	ds_write_b32 v33, v0 offset:17408
	v_cvt_pk_bf16_f32 v0, v9, v1
	v_lshl_add_u32 v7, v17, 1, s12
	ds_write_b32 v34, v0 offset:17408
	ds_write_b32 v88, v18 offset:52236
	ds_write_b32 v7, v6
	ds_write_b32 v82, v4 offset:52236
	v_cvt_pk_bf16_f32 v0, v2, v3
	v_lshl_add_u32 v1, v12, 1, s12
	ds_write_b32 v1, v0
	s_waitcnt lgkmcnt(0)
	s_barrier
	v_readlane_b32 s99, v253, 10
	s_nop 0
	s_add_i32 s99, s76, s99
	s_cmpk_lt_i32 s99, 0x800
	s_cbranch_scc0 .Lgpf_done_next
	v_readlane_b32 s100, v253, 17
	s_lshr_b32 s0, s99, 8
	s_lshl_b32 s0, s0, 12
	s_and_b32 s1, s99, 63
	s_lshl_b32 s101, s1, 6
	s_add_i32 s0, s0, s101
	s_or_b32 s1, s1, s100
	s_bfe_u32 s101, s99, 0x20006
	v_add_u32_e32 v219, s0, v237
	v_lshlrev_b32_e32 v219, 5, v219
	s_lshl_b32 s99, s101, 2
	v_add_u32_e32 v219, s99, v219
	s_lshl_b32 s100, s100, 3
	s_add_i32 s0, s0, s100
	s_lshl_b32 s0, s0, 10
	s_lshl_b32 s101, s101, 8
	s_add_i32 s0, s0, s101
	v_lshlrev_b32_e32 v217, 2, v237
	v_add_u32_e32 v217, s0, v217
	v_add_u32_e32 v218, 0x1000, v217
	s_add_u32 s100, s88, 0x200000
	s_addc_u32 s101, s89, 0
	s_cmp_eq_u32 s1, 0
	s_cbranch_scc1 .Lgpf_zero_next
	global_load_dword v172, v217, s[44:45] offset:-3072 nt
	global_load_dword v173, v217, s[68:69] offset:-3072 nt
	global_load_dword v174, v217, s[72:73] offset:-3072 nt
	global_load_dword v175, v217, s[44:45] offset:-2048 nt
	global_load_dword v176, v217, s[68:69] offset:-2048 nt
	global_load_dword v177, v217, s[72:73] offset:-2048 nt
	global_load_dword v178, v217, s[44:45] offset:-1024 nt
	global_load_dword v179, v217, s[68:69] offset:-1024 nt
	global_load_dword v180, v217, s[72:73] offset:-1024 nt
	s_branch .Lgpf_rest_next

.Lgpf_done_next:
	v_readlane_b32 s0, v253, 51
	v_and_b32_e32 v26, 15, v215
	v_or_b32_e32 v0, s9, v26
	v_mul_u32_u24_e32 v0, 0x110, v0
	v_and_b32_e32 v16, -16, v215
	v_add3_u32 v0, s0, v0, v16
	v_readlane_b32 s0, v253, 52
	ds_read_b128 v[12:15], v0
	ds_read_b128 v[8:11], v0 offset:64
	ds_read_b128 v[4:7], v0 offset:128
	ds_read_b128 v[0:3], v0 offset:192
	v_add_u32_e32 v27, s0, v16
	v_mad_u32_u24 v22, v26, s8, v27
	ds_read_b128 v[16:19], v22
	ds_read_b128 v[28:31], v22 offset:64
	s_waitcnt lgkmcnt(1)
	v_mfma_f32_16x16x32_bf16 v[16:19], v[12:15], v[16:19], 0
	ds_read_b128 v[32:35], v22 offset:128
	v_ashrrev_i32_e32 v23, 4, v215
	v_lshlrev_b32_e32 v25, 2, v23
	s_waitcnt lgkmcnt(1)
	v_mfma_f32_16x16x32_bf16 v[16:19], v[8:11], v[28:31], v[16:19]
	ds_read_b128 v[28:31], v22 offset:192
	v_add_u32_e32 v24, s9, v25
	s_add_u32 s0, s78, 0xc000
	s_waitcnt lgkmcnt(1)
	v_mfma_f32_16x16x32_bf16 v[16:19], v[4:7], v[32:35], v[16:19]
	v_lshlrev_b32_e32 v21, 2, v24
	v_lshlrev_b32_e32 v36, 5, v23
	v_lshlrev_b32_e32 v23, 1, v23
	s_waitcnt lgkmcnt(0)
	v_mfma_f32_16x16x32_bf16 v[16:19], v[0:3], v[28:31], v[16:19]
	v_lshl_add_u32 v28, v26, 2, 0
	v_add_u32_e32 v28, 0x1c400, v28
	ds_read_b32 v28, v28
	s_addc_u32 s1, s79, 0
	v_lshrrev_b32_e32 v20, 5, v24
	v_and_b32_e32 v21, 64, v21
	v_and_b32_e32 v22, 32, v36
	v_and_b32_e32 v23, 4, v23
	s_and_b64 vcc, exec, s[56:57]
	s_movk_i32 s34, 0xf600
	s_cbranch_vccz .LBB0_243
	v_cmp_le_i32_e32 vcc, v24, v26
	v_mov_b32_e32 v29, 0
	v_mov_b32_e32 v30, 0
	s_and_saveexec_b64 s[2:3], vcc
	s_cbranch_execz .LBB0_236
	v_lshl_add_u32 v30, v24, 2, 0
	v_add_u32_e32 v30, 0x1c400, v30
	ds_read_b32 v30, v30
	s_waitcnt lgkmcnt(0)
	v_sub_f32_e32 v30, v28, v30
	v_mul_f32_e32 v30, 0x3fb8aa3b, v30
	v_exp_f32_e32 v30, v30
	s_nop 0
	v_mul_f32_e32 v30, v16, v30
	v_cvt_pk_bf16_f32 v30, v30, s0

	.amdhsa_kernel _Z9hymba_fwd6Params
		.amdhsa_group_segment_fixed_size 0
		.amdhsa_private_segment_fixed_size 0
		.amdhsa_kernarg_size 512
		.amdhsa_user_sgpr_count 2
		.amdhsa_user_sgpr_dispatch_ptr 0
		.amdhsa_user_sgpr_queue_ptr 0
		.amdhsa_user_sgpr_kernarg_segment_ptr 1
		.amdhsa_user_sgpr_dispatch_id 0
		.amdhsa_user_sgpr_kernarg_preload_length 0
		.amdhsa_user_sgpr_kernarg_preload_offset 0
		.amdhsa_user_sgpr_private_segment_size 0
		.amdhsa_uses_dynamic_stack 0
		.amdhsa_enable_private_segment 0
		.amdhsa_system_sgpr_workgroup_id_x 1
		.amdhsa_system_sgpr_workgroup_id_y 0
		.amdhsa_system_sgpr_workgroup_id_z 0
		.amdhsa_system_sgpr_workgroup_info 0
		.amdhsa_system_vgpr_workitem_id 2
		.amdhsa_next_free_vgpr 254
		.amdhsa_next_free_sgpr 102
		.amdhsa_accum_offset 256
		.amdhsa_reserve_vcc 1
		.amdhsa_float_round_mode_32 0
		.amdhsa_float_round_mode_16_64 0
		.amdhsa_float_denorm_mode_32 3
		.amdhsa_float_denorm_mode_16_64 3
		.amdhsa_dx10_clamp 1
		.amdhsa_ieee_mode 1
		.amdhsa_fp16_overflow 0
		.amdhsa_tg_split 0
		.amdhsa_exception_fp_ieee_invalid_op 0
		.amdhsa_exception_fp_denorm_src 0
		.amdhsa_exception_fp_ieee_div_zero 0
		.amdhsa_exception_fp_ieee_overflow 0
		.amdhsa_exception_fp_ieee_underflow 0
		.amdhsa_exception_fp_ieee_inexact 0
		.amdhsa_exception_int_div_zero 0
	.end_amdhsa_kernel

amdhsa.kernels:
  - .agpr_count:     0
    .args:
      - .offset:         0
        .size:           256
        .value_kind:     by_value
      - .offset:         256
        .size:           4
        .value_kind:     hidden_block_count_x
      - .offset:         260
        .size:           4
        .value_kind:     hidden_block_count_y
      - .offset:         264
        .size:           4
        .value_kind:     hidden_block_count_z
      - .offset:         268
        .size:           2
        .value_kind:     hidden_group_size_x
      - .offset:         270
        .size:           2
        .value_kind:     hidden_group_size_y
      - .offset:         272
        .size:           2
        .value_kind:     hidden_group_size_z
      - .offset:         274
        .size:           2
        .value_kind:     hidden_remainder_x
      - .offset:         276
        .size:           2
        .value_kind:     hidden_remainder_y
      - .offset:         278
        .size:           2
        .value_kind:     hidden_remainder_z
      - .offset:         296
        .size:           8
        .value_kind:     hidden_global_offset_x
      - .offset:         304
        .size:           8
        .value_kind:     hidden_global_offset_y
      - .offset:         312
        .size:           8
        .value_kind:     hidden_global_offset_z
      - .offset:         320
        .size:           2
        .value_kind:     hidden_grid_dims
      - .offset:         344
        .size:           8
        .value_kind:     hidden_multigrid_sync_arg
      - .offset:         376
        .size:           4
        .value_kind:     hidden_dynamic_lds_size
    .group_segment_fixed_size: 0
    .kernarg_segment_align: 8
    .kernarg_segment_size: 512
    .language:       OpenCL C
    .language_version:
      - 2
      - 0
    .max_flat_workgroup_size: 512
    .name:           _Z9hymba_fwd6Params
    .private_segment_fixed_size: 0
    .sgpr_count:     108
    .sgpr_spill_count: 57
    .symbol:         _Z9hymba_fwd6Params.kd
    .uniform_work_group_size: 1
    .uses_dynamic_stack: false
    .vgpr_count:     254
    .vgpr_spill_count: 0
    .wavefront_size: 64
